# lru_combine output store write-through (last big write before the end-of-scan-phase grid barrier)
# speedup vs baseline: 1.0037x; 1.0014x over previous
; __device__ __forceinline__ unsigned pk2(float lo, float hi) { return f2bf(lo) | (f2bf(hi) << 16); }
; __device__ __forceinline__ float gelu_tanh(float x) { const float y = 0.7978845608028654f * (x + 0.044715f * x * x * x); const float e = __expf(2.0f * y); return x * (1.0f - __builtin_amdgcn_rcpf(1.0f + e)); }
; __device__ __forceinline__ void lru_combine(const Params& P, size_t wi, size_t nw) {
;     unsigned char* ws = P.ws;
;     const v4u* HLOC = (const v4u*)(ws + WS_HLOC); const v4u* PCUM = (const v4u*)(ws + WS_PCUM); const v4u* GATE = (const v4u*)(ws + WS_GATE);
;     const float* HIN = (const float*)(ws + WS_HIN); bf16* Y = (bf16*)((unsigned char*)P.out + OUT_Y);
;     for (size_t i = wi; i < (size_t)T * 64; i += nw) {
;         const size_t t = i >> 6; const int ch0 = (int)(i & 63) * 8;
;         const v4u hl = HLOC[i], pc = PCUM[i], gt = GATE[i];
;         const f32x4 h0 = *(const f32x4*)(HIN + (t >> 6) * 512 + ch0), h1 = *(const f32x4*)(HIN + (t >> 6) * 512 + ch0 + 4);
;         float y[8];
;         y[0] = (bflo(hl.x) + bflo(pc.x) * h0.x) * gelu_tanh(bflo(gt.x)); y[1] = (bfhi(hl.x) + bfhi(pc.x) * h0.y) * gelu_tanh(bfhi(gt.x));
;         y[2] = (bflo(hl.y) + bflo(pc.y) * h0.z) * gelu_tanh(bflo(gt.y)); y[3] = (bfhi(hl.y) + bfhi(pc.y) * h0.w) * gelu_tanh(bfhi(gt.y));
;         y[4] = (bflo(hl.z) + bflo(pc.z) * h1.x) * gelu_tanh(bflo(gt.z)); y[5] = (bfhi(hl.z) + bfhi(pc.z) * h1.y) * gelu_tanh(bfhi(gt.z));
;         y[6] = (bflo(hl.w) + bflo(pc.w) * h1.z) * gelu_tanh(bflo(gt.w)); y[7] = (bfhi(hl.w) + bfhi(pc.w) * h1.w) * gelu_tanh(bfhi(gt.w));
;         v4u o; o.x = pk2(y[0], y[1]); o.y = pk2(y[2], y[3]); o.z = pk2(y[4], y[5]); o.w = pk2(y[6], y[7]);
;         *(v4u*)(Y + t * 1024 + 512 + ch0) = o;
;     }
.LBB0_2048:
	v_lshl_add_u64 v[10:11], s[24:25], 0, v[6:7]
	v_add_co_u32_e32 v12, vcc, 0x1c00000, v10
	v_lshrrev_b32_e32 v4, 1, v2
	s_nop 0
	v_addc_co_u32_e32 v13, vcc, 0, v11, vcc
	v_add_co_u32_e32 v16, vcc, 0x2c00000, v10
	v_and_b32_e32 v1, 0x1f8, v8
	v_and_b32_e32 v4, 0x7f800, v4
	v_addc_co_u32_e32 v17, vcc, 0, v11, vcc
	v_lshl_add_u64 v[18:19], s[18:19], 0, v[4:5]
	v_lshlrev_b32_e32 v4, 2, v1
	v_add_co_u32_e32 v10, vcc, 0x8c00000, v10
	v_and_b32_e32 v20, 0xfffc00, v6
	v_lshl_add_u64 v[28:29], v[18:19], 0, v[4:5]
	v_addc_co_u32_e32 v11, vcc, 0, v11, vcc
	global_load_dwordx4 v[12:15], v[12:13], off
	v_lshlrev_b32_e32 v4, 1, v20
	global_load_dwordx4 v[16:19], v[16:17], off
	s_nop 0
	global_load_dwordx4 v[20:23], v[28:29], off offset:16
	global_load_dwordx4 v[24:27], v[10:11], off
	s_nop 0
	global_load_dwordx4 v[28:31], v[28:29], off
	v_lshl_add_u64 v[32:33], s[94:95], 0, v[4:5]
	v_lshlrev_b32_e32 v4, 1, v1
	v_lshl_add_u64 v[10:11], v[32:33], 0, v[4:5]
	v_add_co_u32_e32 v32, vcc, 0x400000, v10
	v_lshl_add_u64 v[2:3], v[2:3], 0, s[16:17]
	s_nop 0
	v_addc_co_u32_e32 v33, vcc, 0, v11, vcc
	v_cmp_lt_u64_e64 s[0:1], s[42:43], v[2:3]
	v_lshl_add_u64 v[6:7], v[6:7], 0, s[20:21]
	v_lshl_add_u64 v[8:9], v[8:9], 0, s[12:13]
	s_or_b64 s[14:15], s[0:1], s[14:15]
	s_waitcnt vmcnt(4)
	v_lshlrev_b32_e32 v11, 16, v13
	v_lshlrev_b32_e32 v10, 16, v12
	v_and_b32_e32 v13, 0xffff0000, v13
	v_and_b32_e32 v12, 0xffff0000, v12
	v_lshlrev_b32_e32 v35, 16, v15
	v_lshlrev_b32_e32 v34, 16, v14
	v_and_b32_e32 v15, 0xffff0000, v15
	v_and_b32_e32 v14, 0xffff0000, v14
	s_waitcnt vmcnt(3)
	v_lshlrev_b32_e32 v37, 16, v17
	v_lshlrev_b32_e32 v36, 16, v16
	v_and_b32_e32 v17, 0xffff0000, v17
	v_and_b32_e32 v16, 0xffff0000, v16
	v_lshlrev_b32_e32 v39, 16, v19
	v_lshlrev_b32_e32 v38, 16, v18
	s_waitcnt vmcnt(2)
	v_mov_b32_e32 v40, v20
	v_mov_b32_e32 v41, v22
	v_and_b32_e32 v19, 0xffff0000, v19
	v_and_b32_e32 v18, 0xffff0000, v18
	v_mov_b32_e32 v22, v21
	s_waitcnt vmcnt(1)
	v_lshlrev_b32_e32 v21, 16, v25
	v_lshlrev_b32_e32 v20, 16, v24
	v_and_b32_e32 v25, 0xffff0000, v25
	v_and_b32_e32 v24, 0xffff0000, v24
	s_waitcnt vmcnt(0)
	v_mov_b32_e32 v42, v28
	v_mov_b32_e32 v43, v30
	v_mov_b32_e32 v30, v29
	v_lshlrev_b32_e32 v29, 16, v27
	v_lshlrev_b32_e32 v28, 16, v26
	v_and_b32_e32 v27, 0xffff0000, v27
	v_and_b32_e32 v26, 0xffff0000, v26
	v_pk_fma_f32 v[34:35], v[40:41], v[38:39], v[34:35]
	v_pk_fma_f32 v[14:15], v[22:23], v[18:19], v[14:15]
	v_mul_f32_e32 v1, 0x3d372713, v20
	v_mul_f32_e32 v18, 0x3d372713, v24
	v_mul_f32_e32 v22, 0x3d372713, v21
	v_pk_fma_f32 v[12:13], v[30:31], v[16:17], v[12:13]
	v_mul_f32_e32 v16, 0x3d372713, v25
	v_mul_f32_e32 v30, 0x3d372713, v28
	v_mul_f32_e32 v38, 0x3d372713, v29
	v_mov_b32_e32 v4, v20
	v_mov_b32_e32 v19, v24
	v_pk_fma_f32 v[10:11], v[42:43], v[36:37], v[10:11]
	v_mov_b32_e32 v23, v21
	v_mov_b32_e32 v17, v25
	v_mov_b32_e32 v31, v28
	v_mul_f32_e32 v36, 0x3d372713, v26
	v_mov_b32_e32 v39, v29
	v_mul_f32_e32 v40, 0x3d372713, v27
	v_mul_f32_e32 v1, v1, v20
	v_mul_f32_e32 v18, v18, v24
	v_mul_f32_e32 v22, v22, v21
	v_mul_f32_e32 v16, v16, v25
	v_mul_f32_e32 v30, v30, v28
	v_mul_f32_e32 v38, v38, v29
	v_mov_b32_e32 v37, v26
	v_mov_b32_e32 v41, v27
	v_mul_f32_e32 v36, v36, v26
	v_mul_f32_e32 v40, v40, v27
	v_fmac_f32_e32 v4, v1, v4
	v_fmac_f32_e32 v19, v18, v19
	v_fmac_f32_e32 v23, v22, v23
	v_fmac_f32_e32 v17, v16, v17
	v_fmac_f32_e32 v31, v30, v31
	v_fmac_f32_e32 v39, v38, v39
	v_fmac_f32_e32 v37, v36, v37
	v_fmac_f32_e32 v41, v40, v41
	v_mul_f32_e32 v1, 0x3f4c422a, v4
	v_mul_f32_e32 v4, 0x3f4c422a, v19
	v_mul_f32_e32 v16, 0x3f4c422a, v23
	v_mul_f32_e32 v17, 0x3f4c422a, v17
	v_mul_f32_e32 v18, 0x3f4c422a, v31
	v_mul_f32_e32 v22, 0x3f4c422a, v39
	v_mul_f32_e32 v19, 0x3f4c422a, v37
	v_mul_f32_e32 v23, 0x3f4c422a, v41
	v_add_f32_e32 v1, v1, v1
	v_add_f32_e32 v4, v4, v4
	v_add_f32_e32 v16, v16, v16
	v_add_f32_e32 v17, v17, v17
	v_add_f32_e32 v18, v18, v18
	v_add_f32_e32 v22, v22, v22
	v_add_f32_e32 v19, v19, v19
	v_add_f32_e32 v23, v23, v23
	v_mul_f32_e32 v1, 0x3fb8aa3b, v1
	v_mul_f32_e32 v4, 0x3fb8aa3b, v4
	v_mul_f32_e32 v16, 0x3fb8aa3b, v16
	v_mul_f32_e32 v17, 0x3fb8aa3b, v17
	v_mul_f32_e32 v18, 0x3fb8aa3b, v18
	v_mul_f32_e32 v22, 0x3fb8aa3b, v22
	v_mul_f32_e32 v19, 0x3fb8aa3b, v19
	v_mul_f32_e32 v23, 0x3fb8aa3b, v23
	v_exp_f32_e32 v1, v1
	v_exp_f32_e32 v4, v4
	v_exp_f32_e32 v16, v16
	v_exp_f32_e32 v17, v17
	v_exp_f32_e32 v18, v18
	v_exp_f32_e32 v22, v22
	v_exp_f32_e32 v19, v19
	v_exp_f32_e32 v23, v23
	v_add_f32_e32 v1, 1.0, v1
	v_add_f32_e32 v4, 1.0, v4
	v_add_f32_e32 v30, 1.0, v16
	v_add_f32_e32 v31, 1.0, v17
	v_add_f32_e32 v36, 1.0, v18
	v_add_f32_e32 v38, 1.0, v22
	v_add_f32_e32 v37, 1.0, v19
	v_add_f32_e32 v39, 1.0, v23
	v_rcp_f32_e32 v16, v1
	v_rcp_f32_e32 v18, v4
	v_rcp_f32_e32 v17, v30
	v_rcp_f32_e32 v19, v31
	v_rcp_f32_e32 v22, v36
	v_rcp_f32_e32 v23, v38
	v_rcp_f32_e32 v30, v37
	v_rcp_f32_e32 v31, v39
	v_pk_add_f32 v[16:17], v[16:17], 1.0 op_sel_hi:[1,0] neg_lo:[1,0] neg_hi:[1,0]
	v_pk_add_f32 v[18:19], v[18:19], 1.0 op_sel_hi:[1,0] neg_lo:[1,0] neg_hi:[1,0]
	v_pk_add_f32 v[22:23], v[22:23], 1.0 op_sel_hi:[1,0] neg_lo:[1,0] neg_hi:[1,0]
	v_pk_add_f32 v[30:31], v[30:31], 1.0 op_sel_hi:[1,0] neg_lo:[1,0] neg_hi:[1,0]
	v_pk_mul_f32 v[16:17], v[16:17], v[20:21]
	v_pk_mul_f32 v[18:19], v[18:19], v[24:25]
	v_pk_mul_f32 v[20:21], v[22:23], v[28:29]
	v_pk_mul_f32 v[22:23], v[30:31], v[26:27]
	v_pk_mul_f32 v[10:11], v[10:11], v[16:17]
	v_pk_mul_f32 v[12:13], v[12:13], v[18:19]
	v_pk_mul_f32 v[16:17], v[34:35], v[20:21]
	v_pk_mul_f32 v[14:15], v[14:15], v[22:23]
	v_bfe_u32 v18, v13, 16, 1
	v_bfe_u32 v19, v12, 16, 1
	v_bfe_u32 v20, v10, 16, 1
	v_bfe_u32 v21, v11, 16, 1
	v_bfe_u32 v22, v16, 16, 1
	v_bfe_u32 v23, v17, 16, 1
	v_bfe_u32 v1, v15, 16, 1
	v_bfe_u32 v4, v14, 16, 1
	v_add3_u32 v19, v12, v19, s22
	v_add3_u32 v18, v13, v18, s22
	v_add3_u32 v12, v17, v23, s22
	v_add3_u32 v13, v16, v22, s22
	v_add3_u32 v11, v11, v21, s22
	v_add3_u32 v10, v10, v20, s22
	v_add3_u32 v4, v14, v4, s22
	v_add3_u32 v1, v15, v1, s22
	v_lshrrev_b32_e32 v10, 16, v10
	v_lshrrev_b32_e32 v11, 16, v11
	v_lshrrev_b32_e32 v14, 16, v13
	v_lshrrev_b32_e32 v12, 16, v12
	v_and_or_b32 v13, v1, s3, v12
	v_and_or_b32 v12, v4, s3, v14
	v_and_or_b32 v11, v18, s3, v11
	v_and_or_b32 v10, v19, s3, v10
	global_store_dwordx4 v[32:33], v[10:13], off offset:1024 sc0 sc1
	s_andn2_b64 exec, exec, s[14:15]
	s_cbranch_execnz .LBB0_2048
